# MLA tile loop: QK as two 6-MFMA chains, next-tile DMA issued inside the QK block with SGPR-base addressing, fewer VALU address ops; grid barrier polls the top generation word, L1 invalidate at arrival
# speedup vs baseline: 1.0186x; 1.0084x over previous
; __device__ __forceinline__ unsigned xb_ld(unsigned* p)              { return __hip_atomic_load(p, __ATOMIC_RELAXED, __HIP_MEMORY_SCOPE_AGENT); }
; __device__ __forceinline__ unsigned xb_add(unsigned* p, unsigned v) { return __hip_atomic_fetch_add(p, v, __ATOMIC_RELAXED, __HIP_MEMORY_SCOPE_AGENT); }
; #define XB_SPIN(cond, bar) do { unsigned _sp = 0; while (cond) { __builtin_amdgcn_s_sleep(1); \
;     if ((++_sp & 255u) == 0u) { if (xb_ld(&(bar)[XB_TMO])) break; if (_sp > XB_SPIN_CAP) { atomicAdd(&(bar)[XB_TMO], 1u); break; } } } } while (0)
; __device__ __forceinline__ void xcd_barrier(const XcdBarrier& b) {
;     ...
;         unsigned nloc = b.st[0], nx = b.st[1];
;         if (nloc == 0u) { xcd_barrier_complete(bar, b.x, nloc, nx); b.st[0] = nloc; b.st[1] = nx; }
;         const unsigned old = xb_add(&bar[XB_XSUB(b.x)], 1u);
;         const unsigned gen = old / nloc;
;         if (old + 1u == (gen + 1u) * nloc) {
;             __builtin_amdgcn_fence(__ATOMIC_RELEASE, "agent");
;             asm volatile("s_waitcnt vmcnt(0)" ::: "memory");
;             const unsigned og = xb_add(&bar[XB_TOP], 1u);
;             const unsigned tg = og / nx;
;             if (og + 1u == (tg + 1u) * nx) xb_add(&bar[XB_TOPGEN], 1u);
;             else XB_SPIN(xb_ld(&bar[XB_TOPGEN]) == tg, bar);
;             __builtin_amdgcn_fence(__ATOMIC_ACQUIRE, "agent");
;             xb_add(&bar[XB_XGEN(b.x)], 1u);
;             asm volatile("s_waitcnt vmcnt(0)" ::: "memory");
;         } else {
;             XB_SPIN(xb_ld(&bar[XB_XGEN(b.x)]) == gen, bar);
.LBB0_254:
	s_lshl_b32 s3, s3, 6
	s_add_i32 s6, s3, 0x500
	s_mov_b32 s7, 0
	s_lshl_b64 s[4:5], s[6:7], 2
	s_add_u32 s4, s38, s4
	s_addc_u32 s5, s39, s5
	v_mov_b32_e32 v1, 1
	v_mov_b64_e32 v[6:7], s[4:5]
	flat_atomic_add v1, v[6:7], v1 sc0
	buffer_inv sc1
	v_cvt_f32_u32_e32 v3, v4
	v_sub_u32_e32 v5, 0, v4
	v_rcp_iflag_f32_e32 v3, v3
	s_nop 0
	v_mul_f32_e32 v3, 0x4f7ffffe, v3
	v_cvt_u32_f32_e32 v3, v3
	v_mul_lo_u32 v5, v5, v3
	v_mul_hi_u32 v5, v3, v5
	v_add_u32_e32 v3, v3, v5
	s_waitcnt vmcnt(0) lgkmcnt(0)
	v_mul_hi_u32 v3, v1, v3
	v_mul_lo_u32 v5, v3, v4
	v_add_u32_e32 v6, 1, v1
	v_sub_u32_e32 v1, v1, v5
	v_add_u32_e32 v7, 1, v3
	v_cmp_ge_u32_e32 vcc, v1, v4
	v_sub_u32_e32 v5, v1, v4
	s_nop 0
	v_cndmask_b32_e32 v3, v3, v7, vcc
	v_cndmask_b32_e32 v1, v1, v5, vcc
	v_add_u32_e32 v5, 1, v3
	v_cmp_ge_u32_e32 vcc, v1, v4
	s_nop 1
	v_cndmask_b32_e32 v1, v3, v5, vcc
	v_mad_u64_u32 v[4:5], s[4:5], v4, v1, v[4:5]
	v_cmp_ne_u32_e32 vcc, v6, v4
	s_and_saveexec_b64 s[4:5], vcc
	s_xor_b64 s[4:5], exec, s[4:5]
	s_cbranch_execz .LBB0_267
	s_add_i32 s6, s3, 0x900
	s_lshl_b64 s[6:7], s[6:7], 2
	s_add_u32 s8, s38, 0x3500
	s_addc_u32 s9, s39, 0
	v_mov_b64_e32 v[2:3], s[8:9]
	flat_load_dword v2, v[2:3] sc1
	s_waitcnt vmcnt(0) lgkmcnt(0)
	v_cmp_eq_u32_e32 vcc, v2, v1
	s_and_saveexec_b64 s[6:7], vcc
	s_cbranch_execz .LBB0_266
	s_mov_b32 s26, 1
	s_mov_b64 s[10:11], 0
	s_branch .LBB0_258

; __device__ __forceinline__ unsigned xb_ld(unsigned* p)              { return __hip_atomic_load(p, __ATOMIC_RELAXED, __HIP_MEMORY_SCOPE_AGENT); }
; __device__ __forceinline__ unsigned xb_add(unsigned* p, unsigned v) { return __hip_atomic_fetch_add(p, v, __ATOMIC_RELAXED, __HIP_MEMORY_SCOPE_AGENT); }
; #define XB_SPIN(cond, bar) do { unsigned _sp = 0; while (cond) { __builtin_amdgcn_s_sleep(1); \
;     if ((++_sp & 255u) == 0u) { if (xb_ld(&(bar)[XB_TMO])) break; if (_sp > XB_SPIN_CAP) { atomicAdd(&(bar)[XB_TMO], 1u); break; } } } } while (0)
; __device__ __forceinline__ void xcd_barrier(const XcdBarrier& b) {
;     ...
;         unsigned nloc = b.st[0], nx = b.st[1];
;         if (nloc == 0u) { xcd_barrier_complete(bar, b.x, nloc, nx); b.st[0] = nloc; b.st[1] = nx; }
;         const unsigned old = xb_add(&bar[XB_XSUB(b.x)], 1u);
;         const unsigned gen = old / nloc;
;         if (old + 1u == (gen + 1u) * nloc) {
;             __builtin_amdgcn_fence(__ATOMIC_RELEASE, "agent");
;             asm volatile("s_waitcnt vmcnt(0)" ::: "memory");
;             const unsigned og = xb_add(&bar[XB_TOP], 1u);
;             const unsigned tg = og / nx;
;             if (og + 1u == (tg + 1u) * nx) xb_add(&bar[XB_TOPGEN], 1u);
;             else XB_SPIN(xb_ld(&bar[XB_TOPGEN]) == tg, bar);
;             __builtin_amdgcn_fence(__ATOMIC_ACQUIRE, "agent");
;             xb_add(&bar[XB_XGEN(b.x)], 1u);
;             asm volatile("s_waitcnt vmcnt(0)" ::: "memory");
;         } else {
;             XB_SPIN(xb_ld(&bar[XB_XGEN(b.x)]) == gen, bar);
.LBB0_612:
	s_lshl_b32 s2, s2, 6
	s_add_i32 s88, s2, 0x500
	s_lshl_b64 s[6:7], s[88:89], 2
	s_add_u32 s6, s44, s6
	s_addc_u32 s7, s45, s7
	v_mov_b64_e32 v[4:5], s[6:7]
	flat_atomic_add v3, v[4:5], v235 sc0
	buffer_inv sc1
	v_cvt_f32_u32_e32 v4, v2
	v_sub_u32_e32 v5, 0, v2
	v_rcp_iflag_f32_e32 v4, v4
	s_nop 0
	v_mul_f32_e32 v4, 0x4f7ffffe, v4
	v_cvt_u32_f32_e32 v4, v4
	v_mul_lo_u32 v5, v5, v4
	v_mul_hi_u32 v5, v4, v5
	v_add_u32_e32 v4, v4, v5
	s_waitcnt vmcnt(0) lgkmcnt(0)
	v_mul_hi_u32 v4, v3, v4
	v_mul_lo_u32 v5, v4, v2
	v_add_u32_e32 v6, 1, v3
	v_sub_u32_e32 v3, v3, v5
	v_add_u32_e32 v7, 1, v4
	v_sub_u32_e32 v5, v3, v2
	v_cmp_ge_u32_e32 vcc, v3, v2
	s_nop 1
	v_cndmask_b32_e32 v4, v4, v7, vcc
	v_cndmask_b32_e32 v3, v3, v5, vcc
	v_add_u32_e32 v5, 1, v4
	v_cmp_ge_u32_e32 vcc, v3, v2
	s_nop 1
	v_cndmask_b32_e32 v3, v4, v5, vcc
	v_mad_u64_u32 v[4:5], s[6:7], v2, v3, v[2:3]
	v_cmp_ne_u32_e32 vcc, v6, v4
	s_and_saveexec_b64 s[6:7], vcc
	s_xor_b64 s[8:9], exec, s[6:7]
	s_cbranch_execz .LBB0_625
	s_add_i32 s88, s2, 0x900
	s_lshl_b64 s[6:7], s[88:89], 2
	s_add_u32 s12, s44, 0x3500
	s_addc_u32 s13, s45, 0
	v_mov_b64_e32 v[4:5], s[12:13]
	flat_load_dword v0, v[4:5] sc1
	s_waitcnt vmcnt(0) lgkmcnt(0)
	v_cmp_eq_u32_e32 vcc, v0, v3
	s_and_saveexec_b64 s[10:11], vcc
	s_cbranch_execz .LBB0_624
	s_mov_b32 s3, 1
	s_mov_b64 s[14:15], 0
	s_branch .LBB0_616

; __device__ __forceinline__ unsigned xb_ld(unsigned* p)              { return __hip_atomic_load(p, __ATOMIC_RELAXED, __HIP_MEMORY_SCOPE_AGENT); }
; __device__ __forceinline__ unsigned xb_add(unsigned* p, unsigned v) { return __hip_atomic_fetch_add(p, v, __ATOMIC_RELAXED, __HIP_MEMORY_SCOPE_AGENT); }
; #define XB_SPIN(cond, bar) do { unsigned _sp = 0; while (cond) { __builtin_amdgcn_s_sleep(1); \
;     if ((++_sp & 255u) == 0u) { if (xb_ld(&(bar)[XB_TMO])) break; if (_sp > XB_SPIN_CAP) { atomicAdd(&(bar)[XB_TMO], 1u); break; } } } } while (0)
; __device__ __forceinline__ void xcd_barrier(const XcdBarrier& b) {
;     ...
;         unsigned nloc = b.st[0], nx = b.st[1];
;         if (nloc == 0u) { xcd_barrier_complete(bar, b.x, nloc, nx); b.st[0] = nloc; b.st[1] = nx; }
;         const unsigned old = xb_add(&bar[XB_XSUB(b.x)], 1u);
;         const unsigned gen = old / nloc;
;         if (old + 1u == (gen + 1u) * nloc) {
;             __builtin_amdgcn_fence(__ATOMIC_RELEASE, "agent");
;             asm volatile("s_waitcnt vmcnt(0)" ::: "memory");
;             const unsigned og = xb_add(&bar[XB_TOP], 1u);
;             const unsigned tg = og / nx;
;             if (og + 1u == (tg + 1u) * nx) xb_add(&bar[XB_TOPGEN], 1u);
;             else XB_SPIN(xb_ld(&bar[XB_TOPGEN]) == tg, bar);
;             __builtin_amdgcn_fence(__ATOMIC_ACQUIRE, "agent");
;             xb_add(&bar[XB_XGEN(b.x)], 1u);
;             asm volatile("s_waitcnt vmcnt(0)" ::: "memory");
;         } else {
;             XB_SPIN(xb_ld(&bar[XB_XGEN(b.x)]) == gen, bar);
.LBB0_734:
	s_lshl_b32 s2, s2, 6
	s_add_i32 s88, s2, 0x500
	s_lshl_b64 s[6:7], s[88:89], 2
	s_add_u32 s6, s44, s6
	s_addc_u32 s7, s45, s7
	v_mov_b64_e32 v[4:5], s[6:7]
	flat_atomic_add v4, v[4:5], v235 sc0
	buffer_inv sc1
	v_cvt_f32_u32_e32 v3, v2
	v_sub_u32_e32 v5, 0, v2
	v_rcp_iflag_f32_e32 v3, v3
	s_nop 0
	v_mul_f32_e32 v3, 0x4f7ffffe, v3
	v_cvt_u32_f32_e32 v3, v3
	v_mul_lo_u32 v5, v5, v3
	v_mul_hi_u32 v5, v3, v5
	v_add_u32_e32 v3, v3, v5
	s_waitcnt vmcnt(0) lgkmcnt(0)
	v_mul_hi_u32 v3, v4, v3
	v_mul_lo_u32 v5, v3, v2
	v_sub_u32_e32 v5, v4, v5
	v_cmp_ge_u32_e32 vcc, v5, v2
	v_add_u32_e32 v6, 1, v3
	s_nop 0
	v_cndmask_b32_e32 v3, v3, v6, vcc
	v_sub_u32_e32 v6, v5, v2
	v_cndmask_b32_e32 v5, v5, v6, vcc
	v_cmp_ge_u32_e32 vcc, v5, v2
	v_add_u32_e32 v5, 1, v3
	v_add_u32_e32 v6, 1, v4
	v_cndmask_b32_e32 v3, v3, v5, vcc
	v_mad_u64_u32 v[4:5], s[6:7], v2, v3, v[2:3]
	v_cmp_ne_u32_e32 vcc, v6, v4
	s_and_saveexec_b64 s[6:7], vcc
	s_xor_b64 s[8:9], exec, s[6:7]
	s_cbranch_execz .LBB0_747
	s_add_i32 s88, s2, 0x900
	s_lshl_b64 s[6:7], s[88:89], 2
	s_add_u32 s12, s44, 0x3500
	s_addc_u32 s13, s45, 0
	v_mov_b64_e32 v[4:5], s[12:13]
	flat_load_dword v0, v[4:5] sc1
	s_waitcnt vmcnt(0) lgkmcnt(0)
	v_cmp_eq_u32_e32 vcc, v0, v3
	s_and_saveexec_b64 s[10:11], vcc
	s_cbranch_execz .LBB0_746
	s_mov_b32 s3, 1
	s_mov_b64 s[14:15], 0
	s_branch .LBB0_738

; #define MLA_WAIT_DYN(nf) do { const int nf_ = (nf); if (nf_ >= 3) MLA_WAITN(3); else if (nf_ == 2) MLA_WAITN(2); else if (nf_ == 1) MLA_WAITN(1); else MLA_WAITN(0); } while (0)
; __device__ __forceinline__ void mla_unit(LAS unsigned char* lds, int tid, const bf16_t* QM, const bf16_t* KN, const bf16_t* KR, const bf16_t* VM, bf16_t* OA, float* OSS, AU u, bool has_next, AU nx, bf16x8 (&qr)[6]) {
;     ...
;     MLA_ADDR(u)
;     const int mych = (q0 >> 6) + (wid >> 1);
;     constexpr int SLOT = MLA_SLOT;
;     ...
;     asm volatile("s_waitcnt vmcnt(0)" : "+v"(qr[0]), "+v"(qr[1]), "+v"(qr[2]), "+v"(qr[3]), "+v"(qr[4]), "+v"(qr[5]));
;     f32x16 o0 = {}, o1 = {}, negm = {}; float mref = 0.f, lsum = 0.f;
;     const int vpo = ((lane >> 4) & 1) * 32 + (lane & 3) * 8 + (4 * hi + ((lane & 15) >> 2)) * 64;
;     MLA_WAIT_DYN((NT < 5 ? NT - 1 : 4) - 1);
; __device__ __forceinline__ void phase_attn(Frame& F) {
;     ...
;       auto unit = [&](int i) { const int p = vcu + (i >> 1) * F.G, bh = p >> 3, s = p & 7; return att::AU{bh >> 3, bh & 7, (i & 1) ? s : 15 - s}; };
;       if (nu > 0) {
;           bf16x8 qr[6];
;           att::mla_prologue(F.lds, F.tid, QM, KN, KR, VM, unit(0), qr);
; #pragma unroll 1
;           for (int i = 0; i < nu; ++i) att::mla_unit(F.lds, F.tid, QM, KN, KR, VM, OA, OSS, unit(i), i + 1 < nu, unit(i + 1 < nu ? i + 1 : i), qr);
.LBB0_779:
	s_lshr_b32 s3, s37, 1
	s_mul_i32 s3, s76, s3
	s_add_i32 s7, s79, s3
	s_and_b32 s3, s7, 7
	s_and_b32 s6, s37, 1
	s_xor_b32 s8, s3, 15
	v_mov_b32_e32 v189, v188
	s_cmp_eq_u32 s6, 0
	s_cselect_b32 s38, s8, s3
	v_readfirstlane_b32 s40, v189
	s_ashr_i32 s39, s40, 6
	s_cmp_lt_i32 s39, 4
	s_cselect_b32 s100, 1, 0
	s_cmp_lg_u32 s38, 0
	s_cselect_b64 s[20:21], -1, 0
	s_cmp_lt_i32 s39, 4
	s_cselect_b64 s[8:9], -1, 0
	s_cmp_gt_i32 s39, 3
	s_cselect_b64 s[16:17], -1, 0
	s_cmp_eq_u32 s38, 0
	s_mov_b64 s[18:19], -1
	s_waitcnt vmcnt(0)
	s_waitcnt vmcnt(0)
	s_cbranch_scc1 .LBB0_785
	s_and_b64 vcc, exec, s[16:17]
	s_cbranch_vccz .LBB0_782
	s_waitcnt vmcnt(6) lgkmcnt(0)
	s_barrier
	s_mov_b64 s[18:19], 0

; #define LAS __attribute__((address_space(3)))
; __device__ __forceinline__ float fexp2(float x) { return __builtin_amdgcn_exp2f(x); }
; __device__ __forceinline__ void mla_issue(LAS unsigned char* lds, int wid, const bf16_t* ksrc, const bf16_t* rsrc, const bf16_t* vsrc, int kt) {
;     LAS unsigned char* sl_ = lds + (kt % NS) * MLA_SLOT;
;     dma16(ksrc + (size_t)kt * 64 * 512, sl_ + wid * 1024); if (wid < 4) dma16(rsrc + (size_t)kt * 64 * 32, sl_ + (8 + wid) * 1024);
;     dma16(vsrc + (size_t)kt * 64 * 512, sl_ + 12288 + wid * 1024);
; }
; __device__ __forceinline__ void mla_unit(LAS unsigned char* lds, int tid, const bf16_t* QM, const bf16_t* KN, const bf16_t* KR, const bf16_t* VM, bf16_t* OA, float* OSS, AU u, bool has_next, AU nx, bf16x8 (&qr)[6]) {
;     ...
;     for (int j = 0; j < NT; ++j) {
;         const LAS unsigned char* sl = lds + (j % NS) * SLOT; const LAS unsigned char* sn = lds + ((j + 1) % NS) * SLOT;
;         if (j <= mych) {
;             f32x16 z0, z1;
;             z0 = __builtin_amdgcn_mfma_f32_32x32x16_bf16(kf[0], qr[0], negm, 0, 0, 0); z1 = __builtin_amdgcn_mfma_f32_32x32x16_bf16(kf[1], qr[0], negm, 0, 0, 0);
; #pragma unroll
;             for (int d0 = 1; d0 < 6; ++d0) { z0 = __builtin_amdgcn_mfma_f32_32x32x16_bf16(kf[2 * d0], qr[d0], z0, 0, 0, 0); z1 = __builtin_amdgcn_mfma_f32_32x32x16_bf16(kf[2 * d0 + 1], qr[d0], z1, 0, 0, 0); }
;             bf16x8 vf[8];
;             v_load(vf, sl + 12288 + vpo);
;             __builtin_amdgcn_sched_barrier(0);
;     ...
;             if (j == 0) MLA_MOVE_REF(true);
;             float one = 1.f; asm("" : "+v"(one));
;             float ps = 0.f, pb = 0.f;
; #pragma unroll
;             for (int r = 0; r < 16; ++r) { z0[r] = fexp2(z0[r]); ps = __builtin_fmaf(z0[r], one, ps); z1[r] = fexp2(z1[r]); pb += z1[r]; }
.LBB0_816:
	s_andn2_b64 vcc, exec, s[34:35]
	s_cbranch_vccnz .LBB0_818
	s_waitcnt vmcnt(9) lgkmcnt(0)
	s_barrier
.LBB0_818:
	s_branch .LBB0_822
.LBB0_822:
	s_and_b32 s20, s42, 7
	s_lshl_b32 s44, s20, 7
	s_add_i32 s20, 0, 0x8000
	s_add_i32 s34, s43, 4
	v_add3_u32 v0, v205, s20, v206
	s_add_i32 s35, s41, 0
	s_lshl_b64 s[20:21], s[22:23], 18
	s_add_u32 s20, s20, 0x1b606000
	v_add3_u32 v217, v0, v204, v187
	s_addc_u32 s21, s21, 0
	v_lshl_or_b32 v0, v208, 6, s20
	s_lshr_b32 s20, s40, 2
	s_lshl_b64 s[22:23], s[22:23], 22
	v_and_or_b32 v14, s20, 48, v0
	s_add_u32 s20, s22, 0x20860000
	v_mov_b32_e32 v15, s21
	s_addc_u32 s21, s23, 0
	v_add_lshl_u32 v0, v186, s28, 10
	s_lshl_b64 s[26:27], s[26:27], 1
	v_lshl_add_u64 v[2:3], s[20:21], 0, v[0:1]
	s_add_u32 s21, s26, s44
	s_addc_u32 s26, s27, 0
	s_add_u32 s21, s22, s21
	v_and_b32_e32 v0, 3, v189
	s_addc_u32 s23, s23, s26
	v_lshlrev_b32_e32 v0, 4, v0
	s_add_u32 s22, s21, 0x1e860000
	v_or3_b32 v2, v2, s44, v0
	v_lshlrev_b32_e32 v0, 10, v208
	s_addc_u32 s23, s23, 0
	s_mov_b32 s29, 6
	s_mov_b32 s41, 6
	s_mov_b32 s42, 2
	s_mov_b32 s20, 1
	v_lshl_add_u64 v[204:205], s[30:31], 1, v[2:3]
	v_lshl_add_u64 v[206:207], s[22:23], 0, v[0:1]
	s_add_i32 s43, s43, 3
	v_add_u32_e32 v0, 0, v218
	v_add_u32_e32 v242, v215, v218
	s_mov_b32 s22, 0
	s_mov_b32 s23, -1
	s_branch .LBB0_825
.LBB0_824:
	s_mov_b64 s[26:27], 0x1000
	s_addk_i32 s22, 0x5000
	s_add_i32 s29, s29, 1
	v_add_u32_e32 v14, 0x1000, v14
	s_mov_b64 s[26:27], 0x10000
	s_add_i32 s41, s41, 1
	s_add_i32 s23, s23, -1
	s_add_i32 s42, s42, 1
	s_add_i32 s20, s20, -5
	v_add_u32_e32 v204, 0x10000, v204
	s_cmp_eq_u32 s34, s20
	v_add_u32_e32 v206, 0x10000, v206
	s_cbranch_scc1 .LBB0_857
.LBB0_825:
	s_add_i32 s26, s41, -5
	s_cmp_gt_i32 s26, s6
	s_cbranch_scc1 .LBB0_828
	v_mfma_f32_32x32x16_bf16 v[80:95], v[132:135], v[96:99], v[32:47]
	s_mul_hi_u32 s20, s20, 0xaaaaaaab
	s_lshr_b32 s20, s20, 2
	s_mul_i32 s20, s20, 0x1e000
	s_sub_i32 s20, s22, s20
	v_add_u32_e32 v4, s20, v217
	s_add_i32 s21, s26, 5
	s_cmp_lt_u32 s21, s34
	s_cselect_b32 s101, 1, 0
	ds_read_b64_tr_b16 v[180:181], v4 offset:0
	ds_read_b64_tr_b16 v[182:183], v4 offset:512
	ds_read_b64_tr_b16 v[184:185], v4 offset:4096
	ds_read_b64_tr_b16 v[186:187], v4 offset:4608
	v_mfma_f32_32x32x16_bf16 v[80:95], v[124:127], v[100:103], v[80:95]
	ds_read_b64_tr_b16 v[172:173], v4 offset:1024
	ds_read_b64_tr_b16 v[174:175], v4 offset:1536
	ds_read_b64_tr_b16 v[176:177], v4 offset:5120
	ds_read_b64_tr_b16 v[178:179], v4 offset:5632
	v_mfma_f32_32x32x16_bf16 v[80:95], v[148:151], v[104:107], v[80:95]
	ds_read_b64_tr_b16 v[10:11], v4 offset:2048
	ds_read_b64_tr_b16 v[12:13], v4 offset:2560
	ds_read_b64_tr_b16 v[168:169], v4 offset:6144
	ds_read_b64_tr_b16 v[170:171], v4 offset:6656
	v_mfma_f32_32x32x16_bf16 v[80:95], v[140:143], v[108:111], v[80:95]
	ds_read_b64_tr_b16 v[6:7], v4 offset:3072
	ds_read_b64_tr_b16 v[8:9], v4 offset:3584
	ds_read_b64_tr_b16 v[2:3], v4 offset:7168
	ds_read_b64_tr_b16 v[4:5], v4 offset:7680
	v_mfma_f32_32x32x16_bf16 v[80:95], v[164:167], v[112:115], v[80:95]
	s_cmp_eq_u32 s101, 0
	s_cbranch_scc1 .Lmla_nok
	s_mul_hi_u32 s21, s29, 0xaaaaaaab
	s_lshr_b32 s21, s21, 2
	s_mul_i32 s21, s21, 0x1e000
	s_sub_i32 s21, s22, s21
	s_add_i32 s21, s21, s35
	s_add_i32 s27, s21, 0x1e000
	s_mov_b32 s20, m0
	s_mov_b32 m0, s27
	s_nop 0
	global_load_lds_dwordx4 v206, s[74:75]
	s_mov_b32 m0, s20
.Lmla_nok:
	v_mfma_f32_32x32x16_bf16 v[80:95], v[152:155], v[116:119], v[80:95]
	v_mfma_f32_32x32x16_bf16 v[64:79], v[128:131], v[96:99], v[32:47]
	s_and_b32 s27, s101, s100
	s_cmp_eq_u32 s27, 0
	s_cbranch_scc1 .Lmla_nokr
	s_add_i32 s27, s21, 0x20000
	s_mov_b32 s20, m0
	s_mov_b32 m0, s27
	s_nop 0
	global_load_lds_dwordx4 v14, s[74:75]
	s_mov_b32 m0, s20
.Lmla_nokr:
	v_mfma_f32_32x32x16_bf16 v[64:79], v[120:123], v[100:103], v[64:79]
	s_cmp_eq_u32 s101, 0
	s_cbranch_scc1 .Lmla_nov
	s_add_i32 s27, s21, 0x21000
	s_mov_b32 s20, m0
	s_mov_b32 m0, s27
	s_nop 0
	global_load_lds_dwordx4 v204, s[74:75]
	s_mov_b32 m0, s20
; __device__ __forceinline__ float fexp2(float x) { return __builtin_amdgcn_exp2f(x); }
; __device__ __forceinline__ bf16x8 pfrag(const f32x16& w, int b8) { u32x4 u; u.x = cvtpk(w[b8], w[b8 + 1]); u.y = cvtpk(w[b8 + 2], w[b8 + 3]); u.z = cvtpk(w[b8 + 4], w[b8 + 5]); u.w = cvtpk(w[b8 + 6], w[b8 + 7]); return __builtin_bit_cast(bf16x8, u); }
; #define V_WAIT(vf) asm volatile("s_waitcnt lgkmcnt(0)" : "+v"(vf[0]), "+v"(vf[1]), "+v"(vf[2]), "+v"(vf[3]), "+v"(vf[4]), "+v"(vf[5]), "+v"(vf[6]), "+v"(vf[7]))
; __device__ __forceinline__ void mla_unit(LAS unsigned char* lds, int tid, const bf16_t* QM, const bf16_t* KN, const bf16_t* KR, const bf16_t* VM, bf16_t* OA, float* OSS, AU u, bool has_next, AU nx, bf16x8 (&qr)[6]) {
;     ...
;             float one = 1.f; asm("" : "+v"(one));
;             float ps = 0.f, pb = 0.f;
; #pragma unroll
;             for (int r = 0; r < 16; ++r) { z0[r] = fexp2(z0[r]); ps = __builtin_fmaf(z0[r], one, ps); z1[r] = fexp2(z1[r]); pb += z1[r]; }
;             ps += pb;
;             if (__builtin_expect(__any(!(ps < 1.8446744e19f)), 0)) {
;                 z0 = __builtin_amdgcn_mfma_f32_32x32x16_bf16(kf[0], qr[0], negm, 0, 0, 0); z1 = __builtin_amdgcn_mfma_f32_32x32x16_bf16(kf[1], qr[0], negm, 0, 0, 0);
; #pragma unroll
;                 for (int d0 = 1; d0 < 6; ++d0) { z0 = __builtin_amdgcn_mfma_f32_32x32x16_bf16(kf[2 * d0], qr[d0], z0, 0, 0, 0); z1 = __builtin_amdgcn_mfma_f32_32x32x16_bf16(kf[2 * d0 + 1], qr[d0], z1, 0, 0, 0); }
;                 MLA_MOVE_REF(false);
;                 ps = 0.f;
; #pragma unroll
;                 for (int r = 0; r < 16; ++r) { z0[r] = fexp2(z0[r]); z1[r] = fexp2(z1[r]); ps += z0[r] + z1[r]; }
;             }
;     ...
;             lsum += ps;
;             __builtin_amdgcn_sched_barrier(0);
;             V_WAIT(vf);
; #pragma unroll
;             for (int ks2 = 0; ks2 < 4; ++ks2) {
;                 const bf16x8 pf = pfrag(ks2 < 2 ? z0 : z1, 8 * (ks2 & 1));
;                 o0 = __builtin_amdgcn_mfma_f32_32x32x16_bf16(vf[2 * ks2], pf, o0, 0, 0, 0);
;                 o1 = __builtin_amdgcn_mfma_f32_32x32x16_bf16(vf[2 * ks2 + 1], pf, o1, 0, 0, 0);
;                 if (ks2 < 3) mla_kload(kf, sn, r32, hi, ks2);
.Lmla_nov:
	v_mfma_f32_32x32x16_bf16 v[64:79], v[144:147], v[104:107], v[64:79]
	s_nop 4
	v_exp_f32_e32 v220, v80
	v_exp_f32_e32 v221, v81
	v_exp_f32_e32 v80, v82
	v_mfma_f32_32x32x16_bf16 v[64:79], v[136:139], v[108:111], v[64:79]
	v_exp_f32_e32 v81, v83
	v_exp_f32_e32 v82, v84
	v_exp_f32_e32 v83, v85
	v_mfma_f32_32x32x16_bf16 v[64:79], v[160:163], v[112:115], v[64:79]
	v_exp_f32_e32 v84, v86
	v_exp_f32_e32 v85, v87
	v_exp_f32_e32 v86, v88
	v_mfma_f32_32x32x16_bf16 v[64:79], v[156:159], v[116:119], v[64:79]
	v_add_f32_e32 v191, 0, v220
	v_exp_f32_e32 v87, v89
	v_add_f32_e32 v191, v221, v191
	v_exp_f32_e32 v88, v90
	v_add_f32_e32 v191, v80, v191
	v_exp_f32_e32 v89, v91
	v_add_f32_e32 v191, v81, v191
	v_exp_f32_e32 v90, v92
	v_add_f32_e32 v191, v82, v191
	v_exp_f32_e32 v91, v93
	v_add_f32_e32 v191, v83, v191
	v_exp_f32_e32 v92, v94
	v_add_f32_e32 v191, v84, v191
	v_exp_f32_e32 v94, v95
	v_add_f32_e32 v191, v85, v191
	v_add_f32_e32 v191, v86, v191
	v_add_f32_e32 v191, v87, v191
	v_add_f32_e32 v191, v88, v191
	v_add_f32_e32 v191, v89, v191
	v_add_f32_e32 v191, v90, v191
	v_add_f32_e32 v191, v91, v191
	v_add_f32_e32 v191, v92, v191
	v_add_f32_e32 v191, v94, v191
	v_exp_f32_e32 v218, v64
	v_exp_f32_e32 v219, v65
	v_exp_f32_e32 v64, v66
	v_add_f32_e32 v192, 0, v218
	v_exp_f32_e32 v65, v67
	v_add_f32_e32 v192, v219, v192
	v_exp_f32_e32 v66, v68
	v_add_f32_e32 v192, v64, v192
	v_exp_f32_e32 v67, v69
	v_add_f32_e32 v192, v65, v192
	v_exp_f32_e32 v68, v70
	v_add_f32_e32 v192, v66, v192
	v_exp_f32_e32 v69, v71
	v_add_f32_e32 v192, v67, v192
	v_exp_f32_e32 v70, v72
	v_add_f32_e32 v192, v68, v192
	v_exp_f32_e32 v71, v73
	v_add_f32_e32 v192, v69, v192
	v_exp_f32_e32 v72, v74
	v_add_f32_e32 v192, v70, v192
	v_exp_f32_e32 v73, v75
	v_add_f32_e32 v192, v71, v192
	v_exp_f32_e32 v74, v76
	v_add_f32_e32 v192, v72, v192
	v_exp_f32_e32 v75, v77
	v_add_f32_e32 v192, v73, v192
	v_exp_f32_e32 v76, v78
	v_add_f32_e32 v192, v74, v192
	v_exp_f32_e32 v78, v79
	v_add_f32_e32 v192, v75, v192
	v_add_f32_e32 v192, v76, v192
	v_add_f32_e32 v192, v78, v192
	v_add_f32_e32 v203, v192, v191
	s_mov_b32 s20, 0x5f800000
	v_cmp_ngt_f32_e32 vcc, s20, v203
	s_cbranch_vccnz .LBB0_856
.LBB0_827:
	s_mul_hi_u32 s20, s42, 0xaaaaaaab
	s_lshr_b32 s20, s20, 2
	s_mul_i32 s20, s20, 0x1e000
	s_sub_i32 s20, s22, s20
	v_cvt_pk_bf16_f32 v120, v220, v221
	v_cvt_pk_bf16_f32 v121, v80, v81
	v_cvt_pk_bf16_f32 v122, v82, v83
	v_cvt_pk_bf16_f32 v123, v84, v85
	s_waitcnt lgkmcnt(0)
	v_add_u32_e32 v77, s20, v242
	s_nop 0
	v_mfma_f32_32x32x16_bf16 v[48:63], v[180:183], v[120:123], v[48:63]
	v_mfma_f32_32x32x16_bf16 v[16:31], v[184:187], v[120:123], v[16:31]
	ds_read_b128 v[132:135], v77 offset:40960
	ds_read_b128 v[128:131], v77 offset:41472
	ds_read_b128 v[124:127], v77 offset:43008
	ds_read_b128 v[120:123], v77 offset:43520
	v_cvt_pk_bf16_f32 v80, v86, v87
	v_cvt_pk_bf16_f32 v81, v88, v89
	v_cvt_pk_bf16_f32 v82, v90, v91
	v_cvt_pk_bf16_f32 v83, v92, v94
	ds_read_b128 v[148:151], v77 offset:45056
	ds_read_b128 v[144:147], v77 offset:45568
	ds_read_b128 v[140:143], v77 offset:47104
	ds_read_b128 v[136:139], v77 offset:47616
	v_mfma_f32_32x32x16_bf16 v[48:63], v[172:175], v[80:83], v[48:63]
	v_mfma_f32_32x32x16_bf16 v[16:31], v[176:179], v[80:83], v[16:31]
	v_cvt_pk_bf16_f32 v80, v218, v219
	v_cvt_pk_bf16_f32 v81, v64, v65
	v_cvt_pk_bf16_f32 v82, v66, v67
	v_cvt_pk_bf16_f32 v83, v68, v69
	ds_read_b128 v[164:167], v77 offset:49152
	ds_read_b128 v[160:163], v77 offset:49664
	ds_read_b128 v[152:155], v77 offset:51200
	ds_read_b128 v[156:159], v77 offset:51712
	v_mfma_f32_32x32x16_bf16 v[48:63], v[10:13], v[80:83], v[48:63]
	v_mfma_f32_32x32x16_bf16 v[16:31], v[168:171], v[80:83], v[16:31]
	v_cvt_pk_bf16_f32 v10, v70, v71
	v_cvt_pk_bf16_f32 v11, v72, v73
	v_cvt_pk_bf16_f32 v12, v74, v75
	v_cvt_pk_bf16_f32 v13, v76, v78
	s_nop 1
	v_mfma_f32_32x32x16_bf16 v[48:63], v[6:9], v[10:13], v[48:63]
	v_mfma_f32_32x32x16_bf16 v[16:31], v[2:5], v[10:13], v[16:31]
	v_add_f32_e32 v216, v203, v216

; #define MLA_ISSUE(j) mla_issue(lds, wid, ksrc, rsrc, vsrc, (j))
; #define MLA_WAIT_DYN(nf) do { const int nf_ = (nf); if (nf_ >= 3) MLA_WAITN(3); else if (nf_ == 2) MLA_WAITN(2); else if (nf_ == 1) MLA_WAITN(1); else MLA_WAITN(0); } while (0)
; __device__ __forceinline__ void mla_unit(LAS unsigned char* lds, int tid, const bf16_t* QM, const bf16_t* KN, const bf16_t* KR, const bf16_t* VM, bf16_t* OA, float* OSS, AU u, bool has_next, AU nx, bf16x8 (&qr)[6]) {
;     ...
;         { const int im = (j + 5 < NT - 1) ? j + 5 : NT - 1; MLA_WAIT_DYN(im - (j + 2)); }
;         if (j + 6 < NT) MLA_ISSUE(j + 6);
.LBB0_853:
	s_add_i32 s20, s26, 6
	s_branch .LBB0_824

; __device__ __forceinline__ unsigned xb_ld(unsigned* p)              { return __hip_atomic_load(p, __ATOMIC_RELAXED, __HIP_MEMORY_SCOPE_AGENT); }
; __device__ __forceinline__ unsigned xb_add(unsigned* p, unsigned v) { return __hip_atomic_fetch_add(p, v, __ATOMIC_RELAXED, __HIP_MEMORY_SCOPE_AGENT); }
; #define XB_SPIN(cond, bar) do { unsigned _sp = 0; while (cond) { __builtin_amdgcn_s_sleep(1); \
;     if ((++_sp & 255u) == 0u) { if (xb_ld(&(bar)[XB_TMO])) break; if (_sp > XB_SPIN_CAP) { atomicAdd(&(bar)[XB_TMO], 1u); break; } } } } while (0)
; __device__ __forceinline__ void xcd_barrier(const XcdBarrier& b) {
;     ...
;         unsigned nloc = b.st[0], nx = b.st[1];
;         if (nloc == 0u) { xcd_barrier_complete(bar, b.x, nloc, nx); b.st[0] = nloc; b.st[1] = nx; }
;         const unsigned old = xb_add(&bar[XB_XSUB(b.x)], 1u);
;         const unsigned gen = old / nloc;
;         if (old + 1u == (gen + 1u) * nloc) {
;             __builtin_amdgcn_fence(__ATOMIC_RELEASE, "agent");
;             asm volatile("s_waitcnt vmcnt(0)" ::: "memory");
;             const unsigned og = xb_add(&bar[XB_TOP], 1u);
;             const unsigned tg = og / nx;
;             if (og + 1u == (tg + 1u) * nx) xb_add(&bar[XB_TOPGEN], 1u);
;             else XB_SPIN(xb_ld(&bar[XB_TOPGEN]) == tg, bar);
;             __builtin_amdgcn_fence(__ATOMIC_ACQUIRE, "agent");
;             xb_add(&bar[XB_XGEN(b.x)], 1u);
;             asm volatile("s_waitcnt vmcnt(0)" ::: "memory");
;         } else {
;             XB_SPIN(xb_ld(&bar[XB_XGEN(b.x)]) == gen, bar);
.LBB0_991:
	s_lshl_b32 s2, s2, 6
	s_add_i32 s88, s2, 0x500
	s_lshl_b64 s[6:7], s[88:89], 2
	s_add_u32 s6, s48, s6
	s_addc_u32 s7, s49, s7
	v_mov_b64_e32 v[4:5], s[6:7]
	flat_atomic_add v4, v[4:5], v235 sc0
	buffer_inv sc1
	v_cvt_f32_u32_e32 v3, v2
	v_sub_u32_e32 v5, 0, v2
	v_rcp_iflag_f32_e32 v3, v3
	s_nop 0
	v_mul_f32_e32 v3, 0x4f7ffffe, v3
	v_cvt_u32_f32_e32 v3, v3
	v_mul_lo_u32 v5, v5, v3
	v_mul_hi_u32 v5, v3, v5
	v_add_u32_e32 v3, v3, v5
	s_waitcnt vmcnt(0) lgkmcnt(0)
	v_mul_hi_u32 v3, v4, v3
	v_mul_lo_u32 v5, v3, v2
	v_sub_u32_e32 v5, v4, v5
	v_cmp_ge_u32_e32 vcc, v5, v2
	v_add_u32_e32 v6, 1, v3
	s_nop 0
	v_cndmask_b32_e32 v3, v3, v6, vcc
	v_sub_u32_e32 v6, v5, v2
	v_cndmask_b32_e32 v5, v5, v6, vcc
	v_cmp_ge_u32_e32 vcc, v5, v2
	v_add_u32_e32 v5, 1, v3
	v_add_u32_e32 v6, 1, v4
	v_cndmask_b32_e32 v3, v3, v5, vcc
	v_mad_u64_u32 v[4:5], s[6:7], v2, v3, v[2:3]
	v_cmp_ne_u32_e32 vcc, v6, v4
	s_and_saveexec_b64 s[6:7], vcc
	s_xor_b64 s[10:11], exec, s[6:7]
	s_cbranch_execz .LBB0_1004
	s_add_i32 s88, s2, 0x900
	s_lshl_b64 s[6:7], s[88:89], 2
	s_add_u32 s14, s48, 0x3500
	s_addc_u32 s15, s49, 0
	v_mov_b64_e32 v[4:5], s[14:15]
	flat_load_dword v0, v[4:5] sc1
	s_waitcnt vmcnt(0) lgkmcnt(0)
	v_cmp_eq_u32_e32 vcc, v0, v3
	s_and_saveexec_b64 s[12:13], vcc
	s_cbranch_execz .LBB0_1003
	s_mov_b32 s3, 1
	s_mov_b64 s[16:17], 0
	s_branch .LBB0_995

; __device__ __forceinline__ unsigned xb_ld(unsigned* p)              { return __hip_atomic_load(p, __ATOMIC_RELAXED, __HIP_MEMORY_SCOPE_AGENT); }
; __device__ __forceinline__ unsigned xb_add(unsigned* p, unsigned v) { return __hip_atomic_fetch_add(p, v, __ATOMIC_RELAXED, __HIP_MEMORY_SCOPE_AGENT); }
; #define XB_SPIN(cond, bar) do { unsigned _sp = 0; while (cond) { __builtin_amdgcn_s_sleep(1); \
;     if ((++_sp & 255u) == 0u) { if (xb_ld(&(bar)[XB_TMO])) break; if (_sp > XB_SPIN_CAP) { atomicAdd(&(bar)[XB_TMO], 1u); break; } } } } while (0)
; __device__ __forceinline__ void xcd_barrier(const XcdBarrier& b) {
;     ...
;         unsigned nloc = b.st[0], nx = b.st[1];
;         if (nloc == 0u) { xcd_barrier_complete(bar, b.x, nloc, nx); b.st[0] = nloc; b.st[1] = nx; }
;         const unsigned old = xb_add(&bar[XB_XSUB(b.x)], 1u);
;         const unsigned gen = old / nloc;
;         if (old + 1u == (gen + 1u) * nloc) {
;             __builtin_amdgcn_fence(__ATOMIC_RELEASE, "agent");
;             asm volatile("s_waitcnt vmcnt(0)" ::: "memory");
;             const unsigned og = xb_add(&bar[XB_TOP], 1u);
;             const unsigned tg = og / nx;
;             if (og + 1u == (tg + 1u) * nx) xb_add(&bar[XB_TOPGEN], 1u);
;             else XB_SPIN(xb_ld(&bar[XB_TOPGEN]) == tg, bar);
;             __builtin_amdgcn_fence(__ATOMIC_ACQUIRE, "agent");
;             xb_add(&bar[XB_XGEN(b.x)], 1u);
;             asm volatile("s_waitcnt vmcnt(0)" ::: "memory");
;         } else {
;             XB_SPIN(xb_ld(&bar[XB_XGEN(b.x)]) == gen, bar);
.LBB0_1272:
	s_lshl_b32 s2, s2, 6
	s_add_i32 s88, s2, 0x500
	s_lshl_b64 s[6:7], s[88:89], 2
	s_add_u32 s6, s46, s6
	s_addc_u32 s7, s47, s7
	v_mov_b64_e32 v[4:5], s[6:7]
	flat_atomic_add v4, v[4:5], v235 sc0
	buffer_inv sc1
	v_cvt_f32_u32_e32 v3, v2
	v_sub_u32_e32 v5, 0, v2
	v_rcp_iflag_f32_e32 v3, v3
	s_nop 0
	v_mul_f32_e32 v3, 0x4f7ffffe, v3
	v_cvt_u32_f32_e32 v3, v3
	v_mul_lo_u32 v5, v5, v3
	v_mul_hi_u32 v5, v3, v5
	v_add_u32_e32 v3, v3, v5
	s_waitcnt vmcnt(0) lgkmcnt(0)
	v_mul_hi_u32 v3, v4, v3
	v_mul_lo_u32 v5, v3, v2
	v_sub_u32_e32 v5, v4, v5
	v_cmp_ge_u32_e32 vcc, v5, v2
	v_add_u32_e32 v6, 1, v3
	s_nop 0
	v_cndmask_b32_e32 v3, v3, v6, vcc
	v_sub_u32_e32 v6, v5, v2
	v_cndmask_b32_e32 v5, v5, v6, vcc
	v_cmp_ge_u32_e32 vcc, v5, v2
	v_add_u32_e32 v5, 1, v3
	v_add_u32_e32 v6, 1, v4
	v_cndmask_b32_e32 v3, v3, v5, vcc
	v_mad_u64_u32 v[4:5], s[6:7], v2, v3, v[2:3]
	v_cmp_ne_u32_e32 vcc, v6, v4
	s_and_saveexec_b64 s[6:7], vcc
	s_xor_b64 s[10:11], exec, s[6:7]
	s_cbranch_execz .LBB0_1285
	s_add_i32 s88, s2, 0x900
	s_lshl_b64 s[6:7], s[88:89], 2
	s_add_u32 s14, s46, 0x3500
	s_addc_u32 s15, s47, 0
	v_mov_b64_e32 v[4:5], s[14:15]
	flat_load_dword v0, v[4:5] sc1
	s_waitcnt vmcnt(0) lgkmcnt(0)
	v_cmp_eq_u32_e32 vcc, v0, v3
	s_and_saveexec_b64 s[12:13], vcc
	s_cbranch_execz .LBB0_1284
	s_mov_b32 s3, 1
	s_mov_b64 s[16:17], 0
	s_branch .LBB0_1276

; #define LAS __attribute__((address_space(3)))
; __global__ void __launch_bounds__(NTHREADS, 2) mega_fwd(Params P) {
;     extern __shared__ __attribute__((aligned(16))) unsigned char lds_raw[];
;     Frame F; F.lds = (LAS unsigned char*)lds_raw; F.tid = threadIdx.x; F.lane = F.tid & 63; F.wave = __builtin_amdgcn_readfirstlane(F.tid >> 6); F.G = gridDim.x; F.bx = blockIdx.x; F.P = &P; F.ws = P.ws;
	.amdhsa_kernel _Z8mega_fwd6Params
		.amdhsa_group_segment_fixed_size 0
		.amdhsa_private_segment_fixed_size 0
		.amdhsa_kernarg_size 528
		.amdhsa_user_sgpr_count 2
		.amdhsa_user_sgpr_dispatch_ptr 0
		.amdhsa_user_sgpr_queue_ptr 0
		.amdhsa_user_sgpr_kernarg_segment_ptr 1
		.amdhsa_user_sgpr_dispatch_id 0
		.amdhsa_user_sgpr_kernarg_preload_length 0
		.amdhsa_user_sgpr_kernarg_preload_offset 0
		.amdhsa_user_sgpr_private_segment_size 0
		.amdhsa_uses_dynamic_stack 0
		.amdhsa_enable_private_segment 0
		.amdhsa_system_sgpr_workgroup_id_x 1
		.amdhsa_system_sgpr_workgroup_id_y 0
		.amdhsa_system_sgpr_workgroup_id_z 0
		.amdhsa_system_sgpr_workgroup_info 0
		.amdhsa_system_vgpr_workitem_id 0
		.amdhsa_next_free_vgpr 256
		.amdhsa_next_free_sgpr 102
		.amdhsa_accum_offset 256
		.amdhsa_reserve_vcc 1
		.amdhsa_float_round_mode_32 0
		.amdhsa_float_round_mode_16_64 0
		.amdhsa_float_denorm_mode_32 3
		.amdhsa_float_denorm_mode_16_64 3
		.amdhsa_dx10_clamp 1
		.amdhsa_ieee_mode 1
		.amdhsa_fp16_overflow 0
		.amdhsa_tg_split 0
		.amdhsa_exception_fp_ieee_invalid_op 0
		.amdhsa_exception_fp_denorm_src 0
		.amdhsa_exception_fp_ieee_div_zero 0
		.amdhsa_exception_fp_ieee_overflow 0
		.amdhsa_exception_fp_ieee_underflow 0
		.amdhsa_exception_fp_ieee_inexact 0
		.amdhsa_exception_int_div_zero 0
	.end_amdhsa_kernel

; #define LAS __attribute__((address_space(3)))
; __global__ void __launch_bounds__(NTHREADS, 2) mega_fwd(Params P) {
;     extern __shared__ __attribute__((aligned(16))) unsigned char lds_raw[];
;     Frame F; F.lds = (LAS unsigned char*)lds_raw; F.tid = threadIdx.x; F.lane = F.tid & 63; F.wave = __builtin_amdgcn_readfirstlane(F.tid >> 6); F.G = gridDim.x; F.bx = blockIdx.x; F.P = &P; F.ws = P.ws;
amdhsa.kernels:
  - .agpr_count:     0
    .args:
      - .offset:         0
        .size:           272
        .value_kind:     by_value
      - .offset:         272
        .size:           4
        .value_kind:     hidden_block_count_x
      - .offset:         276
        .size:           4
        .value_kind:     hidden_block_count_y
      - .offset:         280
        .size:           4
        .value_kind:     hidden_block_count_z
      - .offset:         284
        .size:           2
        .value_kind:     hidden_group_size_x
      - .offset:         286
        .size:           2
        .value_kind:     hidden_group_size_y
      - .offset:         288
        .size:           2
        .value_kind:     hidden_group_size_z
      - .offset:         290
        .size:           2
        .value_kind:     hidden_remainder_x
      - .offset:         292
        .size:           2
        .value_kind:     hidden_remainder_y
      - .offset:         294
        .size:           2
        .value_kind:     hidden_remainder_z
      - .offset:         312
        .size:           8
        .value_kind:     hidden_global_offset_x
      - .offset:         320
        .size:           8
        .value_kind:     hidden_global_offset_y
      - .offset:         328
        .size:           8
        .value_kind:     hidden_global_offset_z
      - .offset:         336
        .size:           2
        .value_kind:     hidden_grid_dims
      - .offset:         392
        .size:           4
        .value_kind:     hidden_dynamic_lds_size
    .group_segment_fixed_size: 0
    .kernarg_segment_align: 8
    .kernarg_segment_size: 528
    .language:       OpenCL C
    .language_version:
      - 2
      - 0
    .max_flat_workgroup_size: 512
    .name:           _Z8mega_fwd6Params
    .private_segment_fixed_size: 0
    .sgpr_count:     108
    .sgpr_spill_count: 179
    .symbol:         _Z8mega_fwd6Params.kd
    .uniform_work_group_size: 1
    .uses_dynamic_stack: false
    .vgpr_count:     256
    .vgpr_spill_count: 0
    .wavefront_size: 64
